# s10 + x2 scan: un[] loads of the normaliser recurrence hoisted ahead of the CS stores (tail no longer waits behind the store queue)
# baseline (speedup 1.0000x reference)
; __device__ __forceinline__ void x2_item(int item, int b0, const h16* __restrict__ U, const float* __restrict__ un, const float* __restrict__ amax, const float* __restrict__ blast, ...
;     ...
;     {   const int e2 = sl * 1024 + tid * 2;
;         const h16* up = U + (size_t)lbh * 32 * 8192 + e2; h16* cp = CS + (size_t)lbh * 32 * 8192 + e2;
;         float c0 = 0.f, c1 = 0.f;
;         *(pg8::h16x2*)cp = (pg8::h16x2){(h16)0.f, (h16)0.f};
;         {
; #pragma unroll
;             for (int j = 0; j < 31; ++j) { const float fd = coef[2 * j], fi = coef[2 * j + 1];
;                 c0 = fd * c0 + fi * (float)u[j][0]; c1 = fd * c1 + fi * (float)u[j][1];
;                 *(pg8::h16x2*)(cp + (size_t)(j + 1) * 8192) = (pg8::h16x2){(h16)c0, (h16)c1}; }
;         }
;     }
;     if (sl == 0 && tid < 64) { float n = 0.f; ns[((size_t)gbh * 32) * 64 + tid] = 0.f;
;         float uv[31];
; #pragma unroll
;         for (int c = 0; c < 31; ++c) uv[c] = un[((size_t)gbh * 32 + c) * 64 + tid];
;         asm volatile("" ::: "memory");
; #pragma unroll
;         for (int c = 0; c < 31; ++c) { n = coef[2 * c] * n + coef[2 * c + 1] * uv[c]; ns[((size_t)gbh * 32 + c + 1) * 64 + tid] = n; } }
.LBB0_852:
	s_or_b64 exec, exec, s[14:15]
	s_lshl_b64 s[2:3], s[2:3], 18
	s_lshl_b32 s6, s1, 10
	s_lshl_b64 s[2:3], s[2:3], 1
	v_add_u32_e32 v2, s6, v2
	s_add_u32 s2, s79, s2
	v_ashrrev_i32_e32 v3, 31, v2
	s_addc_u32 s3, s90, s3
	v_lshl_add_u64 v[2:3], v[2:3], 1, s[2:3]
	s_waitcnt lgkmcnt(0)
	s_barrier
	s_cmp_eq_u32 s1, 0
	s_cselect_b64 vcc, -1, 0
	s_and_b64 vcc, vcc, s[38:39]
	s_and_saveexec_b64 s[100:101], vcc
	s_cbranch_execz .Lx2_uv_skip
	v_readlane_b32 s10, v254, 30
	v_readlane_b32 s11, v254, 31
	v_mov_b32_e32 v232, s0
	v_lshlrev_b32_e32 v232, 13, v232
	v_lshl_add_u32 v232, v0, 2, v232
	v_mov_b32_e32 v233, 0
	s_nop 1
	v_lshl_add_u64 v[232:233], s[10:11], 0, v[232:233]
	s_mov_b64 s[10:11], 0x1000
	v_lshl_add_u64 v[234:235], v[232:233], 0, s[10:11]
	global_load_dword v200, v[232:233], off
	global_load_dword v201, v[232:233], off offset:256
	global_load_dword v202, v[232:233], off offset:512
	global_load_dword v203, v[232:233], off offset:768
	global_load_dword v204, v[232:233], off offset:1024
	global_load_dword v205, v[232:233], off offset:1280
	global_load_dword v206, v[232:233], off offset:1536
	global_load_dword v207, v[232:233], off offset:1792
	global_load_dword v208, v[232:233], off offset:2048
	global_load_dword v209, v[232:233], off offset:2304
	global_load_dword v210, v[232:233], off offset:2560
	global_load_dword v211, v[232:233], off offset:2816
	global_load_dword v212, v[232:233], off offset:3072
	global_load_dword v213, v[232:233], off offset:3328
	global_load_dword v214, v[232:233], off offset:3584
	global_load_dword v215, v[232:233], off offset:3840
	global_load_dword v216, v[234:235], off
	global_load_dword v217, v[234:235], off offset:256
	global_load_dword v218, v[234:235], off offset:512
	global_load_dword v219, v[234:235], off offset:768
	global_load_dword v220, v[234:235], off offset:1024
	global_load_dword v221, v[234:235], off offset:1280
	global_load_dword v222, v[234:235], off offset:1536
	global_load_dword v223, v[234:235], off offset:1792
	global_load_dword v224, v[234:235], off offset:2048
	global_load_dword v225, v[234:235], off offset:2304
	global_load_dword v226, v[234:235], off offset:2560
	global_load_dword v227, v[234:235], off offset:2816
	global_load_dword v228, v[234:235], off offset:3072
	global_load_dword v229, v[234:235], off offset:3328
	global_load_dword v230, v[234:235], off offset:3584
.Lx2_uv_skip:
	s_or_b64 exec, exec, s[100:101]
	global_store_dword v[2:3], v97, off
	ds_read_b128 v[36:39], v97
	ds_read_b128 v[40:43], v97 offset:16
	s_waitcnt vmcnt(31)
	v_cvt_f32_f16_sdwa v35, v34 dst_sel:DWORD dst_unused:UNUSED_PAD src0_sel:WORD_1
	v_cvt_f32_f16_e32 v34, v34
	s_movk_i32 s2, 0x4000
	s_waitcnt lgkmcnt(1)
	v_mul_f32_e32 v52, 0, v36
	ds_read_b128 v[44:47], v97 offset:32
	ds_read_b128 v[48:51], v97 offset:48
	v_pk_fma_f32 v[34:35], v[36:37], v[34:35], v[52:53] op_sel:[1,0,0] op_sel_hi:[1,1,0]
	s_waitcnt vmcnt(30)
	v_cvt_f32_f16_sdwa v37, v33 dst_sel:DWORD dst_unused:UNUSED_PAD src0_sel:WORD_1
	v_cvt_f32_f16_e32 v36, v33
	v_add_co_u32_e32 v52, vcc, s2, v2
	s_waitcnt vmcnt(29)
	v_cvt_f32_f16_sdwa v33, v32 dst_sel:DWORD dst_unused:UNUSED_PAD src0_sel:WORD_1
	v_cvt_f32_f16_e32 v32, v32
	v_cvt_pk_f16_f32 v5, v34, v35
	v_addc_co_u32_e32 v53, vcc, 0, v3, vcc
	global_store_dword v[52:53], v5, off
	v_mov_b32_e32 v52, v39
	v_pk_mul_f32 v[36:37], v[52:53], v[36:37] op_sel_hi:[0,1]
	s_mov_b32 s2, 0x8000
	v_pk_fma_f32 v[34:35], v[34:35], v[38:39], v[36:37] op_sel_hi:[1,0,1]
	v_add_co_u32_e32 v36, vcc, s2, v2
	s_waitcnt lgkmcnt(2)
	v_pk_mul_f32 v[32:33], v[40:41], v[32:33] op_sel:[1,0]
	v_cvt_pk_f16_f32 v5, v34, v35
	v_addc_co_u32_e32 v37, vcc, 0, v3, vcc
	v_pk_fma_f32 v[32:33], v[34:35], v[40:41], v[32:33] op_sel_hi:[1,0,1]
	s_waitcnt vmcnt(29)
	v_cvt_f32_f16_sdwa v35, v31 dst_sel:DWORD dst_unused:UNUSED_PAD src0_sel:WORD_1
	v_cvt_f32_f16_e32 v34, v31
	s_mov_b32 s2, 0xc000
	global_store_dword v[36:37], v5, off
	v_add_co_u32_e32 v36, vcc, s2, v2
	s_waitcnt vmcnt(29)
	v_cvt_f32_f16_sdwa v31, v30 dst_sel:DWORD dst_unused:UNUSED_PAD src0_sel:WORD_1
	v_cvt_f32_f16_e32 v30, v30
	v_cvt_pk_f16_f32 v5, v32, v33
	v_addc_co_u32_e32 v37, vcc, 0, v3, vcc
	global_store_dword v[36:37], v5, off
	v_mov_b32_e32 v36, v43
	v_pk_mul_f32 v[34:35], v[36:37], v[34:35] op_sel_hi:[0,1]
	v_pk_fma_f32 v[32:33], v[32:33], v[42:43], v[34:35] op_sel_hi:[1,0,1]
	s_waitcnt lgkmcnt(1)
	v_pk_mul_f32 v[30:31], v[44:45], v[30:31] op_sel:[1,0]
	v_cvt_pk_f16_f32 v5, v32, v33
	v_pk_fma_f32 v[30:31], v[32:33], v[44:45], v[30:31] op_sel_hi:[1,0,1]
	s_waitcnt vmcnt(29)
	v_cvt_f32_f16_sdwa v33, v28 dst_sel:DWORD dst_unused:UNUSED_PAD src0_sel:WORD_1
	v_cvt_f32_f16_e32 v32, v28
	s_mov_b32 s2, 0x10000
	v_add_co_u32_e32 v34, vcc, s2, v2
	v_mov_b32_e32 v28, v47
	s_nop 0
	v_addc_co_u32_e32 v35, vcc, 0, v3, vcc
	s_waitcnt vmcnt(27)
	v_pk_mul_f32 v[32:33], v[28:29], v[32:33] op_sel_hi:[0,1]
	global_store_dword v[34:35], v5, off
	v_cvt_pk_f16_f32 v5, v30, v31
	v_pk_fma_f32 v[30:31], v[30:31], v[46:47], v[32:33] op_sel_hi:[1,0,1]
	v_cvt_f32_f16_sdwa v33, v26 dst_sel:DWORD dst_unused:UNUSED_PAD src0_sel:WORD_1
	v_cvt_f32_f16_e32 v32, v26
	s_mov_b32 s2, 0x14000
	v_add_co_u32_e32 v34, vcc, s2, v2
	s_mov_b32 s2, 0x18000
	s_nop 0
	v_addc_co_u32_e32 v35, vcc, 0, v3, vcc
	s_waitcnt lgkmcnt(0)
	v_pk_mul_f32 v[32:33], v[48:49], v[32:33] op_sel:[1,0]
	global_store_dword v[34:35], v5, off
	v_cvt_pk_f16_f32 v5, v30, v31
	v_add_co_u32_e32 v34, vcc, s2, v2
	v_pk_fma_f32 v[30:31], v[30:31], v[48:49], v[32:33] op_sel_hi:[1,0,1]
	v_cvt_f32_f16_sdwa v33, v29 dst_sel:DWORD dst_unused:UNUSED_PAD src0_sel:WORD_1
	v_cvt_f32_f16_e32 v32, v29
	v_addc_co_u32_e32 v35, vcc, 0, v3, vcc
	s_mov_b32 s2, 0x1c000
	v_add_co_u32_e32 v28, vcc, s2, v2
	global_store_dword v[34:35], v5, off
	v_cvt_pk_f16_f32 v5, v30, v31
	v_addc_co_u32_e32 v29, vcc, 0, v3, vcc
	v_mov_b32_e32 v26, v51
	global_store_dword v[28:29], v5, off
	s_waitcnt vmcnt(30)
; __device__ __forceinline__ void x2_item(int item, int b0, const h16* __restrict__ U, const float* __restrict__ un, const float* __restrict__ amax, const float* __restrict__ blast, ...
;     ...
;     {   const int e2 = sl * 1024 + tid * 2;
;         const h16* up = U + (size_t)lbh * 32 * 8192 + e2; h16* cp = CS + (size_t)lbh * 32 * 8192 + e2;
;         float c0 = 0.f, c1 = 0.f;
;         *(pg8::h16x2*)cp = (pg8::h16x2){(h16)0.f, (h16)0.f};
;         {
; #pragma unroll
;             for (int j = 0; j < 31; ++j) { const float fd = coef[2 * j], fi = coef[2 * j + 1];
;                 c0 = fd * c0 + fi * (float)u[j][0]; c1 = fd * c1 + fi * (float)u[j][1];
;                 *(pg8::h16x2*)(cp + (size_t)(j + 1) * 8192) = (pg8::h16x2){(h16)c0, (h16)c1}; }
;         }
;     }
	v_pk_mul_f32 v[28:29], v[26:27], v[32:33] op_sel_hi:[0,1]
	v_pk_fma_f32 v[36:37], v[30:31], v[50:51], v[28:29] op_sel_hi:[1,0,1]
	ds_read_b128 v[28:31], v97 offset:64
	ds_read_b128 v[32:35], v97 offset:80
	v_cvt_f32_f16_sdwa v39, v27 dst_sel:DWORD dst_unused:UNUSED_PAD src0_sel:WORD_1
	v_cvt_f32_f16_e32 v38, v27
	s_mov_b32 s2, 0x20000
	v_add_co_u32_e32 v26, vcc, s2, v2
	v_cvt_pk_f16_f32 v5, v36, v37
	s_nop 0
	v_addc_co_u32_e32 v27, vcc, 0, v3, vcc
	global_store_dword v[26:27], v5, off
	s_waitcnt lgkmcnt(1)
	v_pk_mul_f32 v[26:27], v[28:29], v[38:39] op_sel:[1,0]
	s_mov_b32 s2, 0x24000
	v_pk_fma_f32 v[26:27], v[36:37], v[28:29], v[26:27] op_sel_hi:[1,0,1]
	s_waitcnt vmcnt(30)
	v_cvt_f32_f16_sdwa v29, v25 dst_sel:DWORD dst_unused:UNUSED_PAD src0_sel:WORD_1
	v_cvt_f32_f16_e32 v28, v25
	v_add_co_u32_e32 v36, vcc, s2, v2
	s_waitcnt vmcnt(29)
	v_cvt_f32_f16_sdwa v25, v24 dst_sel:DWORD dst_unused:UNUSED_PAD src0_sel:WORD_1
	v_cvt_f32_f16_e32 v24, v24
	v_cvt_pk_f16_f32 v5, v26, v27
	v_addc_co_u32_e32 v37, vcc, 0, v3, vcc
	global_store_dword v[36:37], v5, off
	v_mov_b32_e32 v36, v31
	v_pk_mul_f32 v[28:29], v[36:37], v[28:29] op_sel_hi:[0,1]
	s_mov_b32 s2, 0x28000
	v_pk_fma_f32 v[26:27], v[26:27], v[30:31], v[28:29] op_sel_hi:[1,0,1]
	v_add_co_u32_e32 v28, vcc, s2, v2
	s_waitcnt lgkmcnt(0)
	v_pk_mul_f32 v[24:25], v[32:33], v[24:25] op_sel:[1,0]
	v_cvt_pk_f16_f32 v5, v26, v27
	v_addc_co_u32_e32 v29, vcc, 0, v3, vcc
	v_pk_fma_f32 v[24:25], v[26:27], v[32:33], v[24:25] op_sel_hi:[1,0,1]
	s_waitcnt vmcnt(29)
	v_cvt_f32_f16_sdwa v27, v23 dst_sel:DWORD dst_unused:UNUSED_PAD src0_sel:WORD_1
	v_cvt_f32_f16_e32 v26, v23
	s_mov_b32 s2, 0x2c000
	global_store_dword v[28:29], v5, off
	v_add_co_u32_e32 v28, vcc, s2, v2
	v_cvt_pk_f16_f32 v5, v24, v25
	s_nop 0
	v_addc_co_u32_e32 v29, vcc, 0, v3, vcc
	global_store_dword v[28:29], v5, off
	v_mov_b32_e32 v28, v35
	v_pk_mul_f32 v[26:27], v[28:29], v[26:27] op_sel_hi:[0,1]
	s_mov_b32 s2, 0x30000
	v_pk_fma_f32 v[40:41], v[24:25], v[34:35], v[26:27] op_sel_hi:[1,0,1]
	v_add_co_u32_e32 v24, vcc, s2, v2
	v_cvt_pk_f16_f32 v5, v40, v41
	s_nop 0
	v_addc_co_u32_e32 v25, vcc, 0, v3, vcc
	global_store_dword v[24:25], v5, off
	ds_read_b128 v[24:27], v97 offset:96
	s_waitcnt vmcnt(31)
	v_cvt_f32_f16_sdwa v43, v21 dst_sel:DWORD dst_unused:UNUSED_PAD src0_sel:WORD_1
	v_cvt_f32_f16_e32 v42, v21
	s_waitcnt vmcnt(30)
	v_cvt_f32_f16_sdwa v21, v20 dst_sel:DWORD dst_unused:UNUSED_PAD src0_sel:WORD_1
	v_cvt_f32_f16_e32 v20, v20
	s_mov_b32 s2, 0x34000
	s_waitcnt lgkmcnt(0)
	v_pk_mul_f32 v[42:43], v[24:25], v[42:43] op_sel:[1,0]
	ds_read_b128 v[28:31], v97 offset:112
	ds_read_b128 v[32:35], v97 offset:128
	ds_read_b128 v[36:39], v97 offset:144
	v_pk_fma_f32 v[24:25], v[40:41], v[24:25], v[42:43] op_sel_hi:[1,0,1]
	v_add_co_u32_e32 v40, vcc, s2, v2
	v_cvt_pk_f16_f32 v5, v24, v25
	s_nop 0
	v_addc_co_u32_e32 v41, vcc, 0, v3, vcc
	global_store_dword v[40:41], v5, off
	v_mov_b32_e32 v40, v27
	v_pk_mul_f32 v[20:21], v[40:41], v[20:21] op_sel_hi:[0,1]
	v_pk_fma_f32 v[20:21], v[24:25], v[26:27], v[20:21] op_sel_hi:[1,0,1]
	s_waitcnt vmcnt(30)
	v_cvt_f32_f16_sdwa v25, v18 dst_sel:DWORD dst_unused:UNUSED_PAD src0_sel:WORD_1
	v_cvt_f32_f16_e32 v24, v18
	s_waitcnt vmcnt(29)
	v_cvt_f32_f16_sdwa v23, v22 dst_sel:DWORD dst_unused:UNUSED_PAD src0_sel:WORD_1
	v_cvt_f32_f16_e32 v22, v22
	v_add_co_u32_e32 v26, vcc, s96, v2
	s_waitcnt lgkmcnt(2)
	v_pk_mul_f32 v[24:25], v[28:29], v[24:25] op_sel:[1,0]
	v_mov_b32_e32 v18, v31
	v_cvt_pk_f16_f32 v5, v20, v21
	v_addc_co_u32_e32 v27, vcc, 0, v3, vcc
	v_pk_fma_f32 v[20:21], v[20:21], v[28:29], v[24:25] op_sel_hi:[1,0,1]
	s_mov_b32 s2, 0x3c000
	s_waitcnt vmcnt(28)
	v_pk_mul_f32 v[22:23], v[18:19], v[22:23] op_sel_hi:[0,1]
	global_store_dword v[26:27], v5, off
	v_cvt_pk_f16_f32 v5, v20, v21
	v_add_co_u32_e32 v24, vcc, s2, v2
	v_pk_fma_f32 v[20:21], v[20:21], v[30:31], v[22:23] op_sel_hi:[1,0,1]
	v_cvt_f32_f16_sdwa v23, v19 dst_sel:DWORD dst_unused:UNUSED_PAD src0_sel:WORD_1
	v_cvt_f32_f16_e32 v22, v19
	v_addc_co_u32_e32 v25, vcc, 0, v3, vcc
	s_mov_b32 s2, 0x40000
	v_add_co_u32_e32 v18, vcc, s2, v2
	global_store_dword v[24:25], v5, off
	v_cvt_pk_f16_f32 v5, v20, v21
	v_addc_co_u32_e32 v19, vcc, 0, v3, vcc
	global_store_dword v[18:19], v5, off
	s_waitcnt lgkmcnt(1)
	v_pk_mul_f32 v[18:19], v[32:33], v[22:23] op_sel:[1,0]
	s_mov_b32 s2, 0x44000
	v_pk_fma_f32 v[18:19], v[20:21], v[32:33], v[18:19] op_sel_hi:[1,0,1]
	s_waitcnt vmcnt(30)
	v_cvt_f32_f16_sdwa v21, v17 dst_sel:DWORD dst_unused:UNUSED_PAD src0_sel:WORD_1
	v_cvt_f32_f16_e32 v20, v17
	v_add_co_u32_e32 v22, vcc, s2, v2
	s_waitcnt vmcnt(29)
	v_cvt_f32_f16_sdwa v17, v16 dst_sel:DWORD dst_unused:UNUSED_PAD src0_sel:WORD_1
	v_cvt_f32_f16_e32 v16, v16
	v_cvt_pk_f16_f32 v5, v18, v19
	v_addc_co_u32_e32 v23, vcc, 0, v3, vcc
	global_store_dword v[22:23], v5, off
	v_mov_b32_e32 v22, v35
	v_pk_mul_f32 v[20:21], v[22:23], v[20:21] op_sel_hi:[0,1]
	s_mov_b32 s2, 0x48000
	v_pk_fma_f32 v[18:19], v[18:19], v[34:35], v[20:21] op_sel_hi:[1,0,1]
	v_add_co_u32_e32 v20, vcc, s2, v2
	s_waitcnt lgkmcnt(0)
	v_pk_mul_f32 v[16:17], v[36:37], v[16:17] op_sel:[1,0]
	v_cvt_pk_f16_f32 v5, v18, v19
	v_addc_co_u32_e32 v21, vcc, 0, v3, vcc
	v_pk_fma_f32 v[16:17], v[18:19], v[36:37], v[16:17] op_sel_hi:[1,0,1]
	s_waitcnt vmcnt(29)
	v_cvt_f32_f16_sdwa v19, v15 dst_sel:DWORD dst_unused:UNUSED_PAD src0_sel:WORD_1
	v_cvt_f32_f16_e32 v18, v15
	s_mov_b32 s2, 0x4c000
	global_store_dword v[20:21], v5, off
	v_add_co_u32_e32 v20, vcc, s2, v2
	v_cvt_pk_f16_f32 v5, v16, v17
	s_nop 0
	v_addc_co_u32_e32 v21, vcc, 0, v3, vcc
	global_store_dword v[20:21], v5, off
	v_mov_b32_e32 v20, v39
	v_pk_mul_f32 v[18:19], v[20:21], v[18:19] op_sel_hi:[0,1]
	v_pk_fma_f32 v[24:25], v[16:17], v[38:39], v[18:19] op_sel_hi:[1,0,1]
	ds_read_b128 v[16:19], v97 offset:160
	s_waitcnt vmcnt(30)
; __device__ __forceinline__ void x2_item(int item, int b0, const h16* __restrict__ U, const float* __restrict__ un, const float* __restrict__ amax, const float* __restrict__ blast, ...
;     ...
;     {   const int e2 = sl * 1024 + tid * 2;
;         const h16* up = U + (size_t)lbh * 32 * 8192 + e2; h16* cp = CS + (size_t)lbh * 32 * 8192 + e2;
;         float c0 = 0.f, c1 = 0.f;
;         *(pg8::h16x2*)cp = (pg8::h16x2){(h16)0.f, (h16)0.f};
;         {
; #pragma unroll
;             for (int j = 0; j < 31; ++j) { const float fd = coef[2 * j], fi = coef[2 * j + 1];
;                 c0 = fd * c0 + fi * (float)u[j][0]; c1 = fd * c1 + fi * (float)u[j][1];
;                 *(pg8::h16x2*)(cp + (size_t)(j + 1) * 8192) = (pg8::h16x2){(h16)c0, (h16)c1}; }
;         }
;     }
;     if (sl == 0 && tid < 64) { float n = 0.f; ns[((size_t)gbh * 32) * 64 + tid] = 0.f;
	v_cvt_f32_f16_sdwa v15, v14 dst_sel:DWORD dst_unused:UNUSED_PAD src0_sel:WORD_1
	v_cvt_f32_f16_e32 v14, v14
	s_mov_b32 s2, 0x50000
	v_add_co_u32_e32 v20, vcc, s2, v2
	v_cvt_pk_f16_f32 v5, v24, v25
	s_nop 0
	v_addc_co_u32_e32 v21, vcc, 0, v3, vcc
	global_store_dword v[20:21], v5, off
	ds_read_b128 v[20:23], v97 offset:176
	s_waitcnt lgkmcnt(1)
	v_pk_mul_f32 v[14:15], v[16:17], v[14:15] op_sel:[1,0]
	s_waitcnt vmcnt(29)
	v_cvt_f32_f16_sdwa v33, v10 dst_sel:DWORD dst_unused:UNUSED_PAD src0_sel:WORD_1
	v_pk_fma_f32 v[14:15], v[24:25], v[16:17], v[14:15] op_sel_hi:[1,0,1]
	v_cvt_f32_f16_sdwa v17, v12 dst_sel:DWORD dst_unused:UNUSED_PAD src0_sel:WORD_1
	v_cvt_f32_f16_e32 v16, v12
	v_cvt_f32_f16_e32 v32, v10
	s_mov_b32 s2, 0x54000
	v_mov_b32_e32 v12, v19
	v_add_co_u32_e32 v24, vcc, s2, v2
	s_waitcnt vmcnt(28)
	v_pk_mul_f32 v[16:17], v[12:13], v[16:17] op_sel_hi:[0,1]
	v_cvt_pk_f16_f32 v5, v14, v15
	v_addc_co_u32_e32 v25, vcc, 0, v3, vcc
	v_pk_fma_f32 v[18:19], v[14:15], v[18:19], v[16:17] op_sel_hi:[1,0,1]
	s_mov_b32 s2, 0x58000
	s_waitcnt lgkmcnt(0)
	v_pk_mul_f32 v[32:33], v[20:21], v[32:33] op_sel:[1,0]
	global_store_dword v[24:25], v5, off
	v_cvt_pk_f16_f32 v5, v18, v19
	v_add_co_u32_e32 v14, vcc, s2, v2
	v_pk_fma_f32 v[18:19], v[18:19], v[20:21], v[32:33] op_sel_hi:[1,0,1]
	v_cvt_f32_f16_sdwa v21, v13 dst_sel:DWORD dst_unused:UNUSED_PAD src0_sel:WORD_1
	v_cvt_f32_f16_e32 v20, v13
	v_addc_co_u32_e32 v15, vcc, 0, v3, vcc
	s_mov_b32 s2, 0x5c000
	v_add_co_u32_e32 v12, vcc, s2, v2
	global_store_dword v[14:15], v5, off
	v_cvt_pk_f16_f32 v5, v18, v19
	v_addc_co_u32_e32 v13, vcc, 0, v3, vcc
	v_mov_b32_e32 v10, v23
	ds_read_b128 v[14:17], v97 offset:192
	ds_read_b128 v[24:27], v97 offset:208
	ds_read_b128 v[28:31], v97 offset:224
	global_store_dword v[12:13], v5, off
	s_waitcnt vmcnt(30)
	v_pk_mul_f32 v[12:13], v[10:11], v[20:21] op_sel_hi:[0,1]
	v_pk_fma_f32 v[12:13], v[18:19], v[22:23], v[12:13] op_sel_hi:[1,0,1]
	v_cvt_f32_f16_sdwa v19, v11 dst_sel:DWORD dst_unused:UNUSED_PAD src0_sel:WORD_1
	v_cvt_f32_f16_e32 v18, v11
	s_mov_b32 s2, 0x60000
	v_add_co_u32_e32 v10, vcc, s2, v2
	v_cvt_pk_f16_f32 v5, v12, v13
	s_nop 0
	v_addc_co_u32_e32 v11, vcc, 0, v3, vcc
	global_store_dword v[10:11], v5, off
	s_waitcnt lgkmcnt(2)
	v_pk_mul_f32 v[10:11], v[14:15], v[18:19] op_sel:[1,0]
	s_mov_b32 s2, 0x64000
	v_pk_fma_f32 v[10:11], v[12:13], v[14:15], v[10:11] op_sel_hi:[1,0,1]
	s_waitcnt vmcnt(30)
	v_cvt_f32_f16_sdwa v13, v9 dst_sel:DWORD dst_unused:UNUSED_PAD src0_sel:WORD_1
	v_cvt_f32_f16_e32 v12, v9
	v_add_co_u32_e32 v14, vcc, s2, v2
	s_waitcnt vmcnt(29)
	v_cvt_f32_f16_sdwa v9, v8 dst_sel:DWORD dst_unused:UNUSED_PAD src0_sel:WORD_1
	v_cvt_f32_f16_e32 v8, v8
	v_cvt_pk_f16_f32 v5, v10, v11
	v_addc_co_u32_e32 v15, vcc, 0, v3, vcc
	global_store_dword v[14:15], v5, off
	v_mov_b32_e32 v14, v17
	v_pk_mul_f32 v[12:13], v[14:15], v[12:13] op_sel_hi:[0,1]
	s_mov_b32 s2, 0x68000
	v_pk_fma_f32 v[10:11], v[10:11], v[16:17], v[12:13] op_sel_hi:[1,0,1]
	v_add_co_u32_e32 v12, vcc, s2, v2
	s_waitcnt lgkmcnt(1)
	v_pk_mul_f32 v[8:9], v[24:25], v[8:9] op_sel:[1,0]
	v_cvt_pk_f16_f32 v5, v10, v11
	v_addc_co_u32_e32 v13, vcc, 0, v3, vcc
	v_pk_fma_f32 v[8:9], v[10:11], v[24:25], v[8:9] op_sel_hi:[1,0,1]
	s_waitcnt vmcnt(29)
	v_cvt_f32_f16_sdwa v11, v7 dst_sel:DWORD dst_unused:UNUSED_PAD src0_sel:WORD_1
	v_cvt_f32_f16_e32 v10, v7
	s_mov_b32 s2, 0x6c000
	global_store_dword v[12:13], v5, off
	v_add_co_u32_e32 v12, vcc, s2, v2
	v_cvt_pk_f16_f32 v5, v8, v9
	s_nop 0
	v_addc_co_u32_e32 v13, vcc, 0, v3, vcc
	s_waitcnt vmcnt(29)
	v_cvt_f32_f16_sdwa v7, v6 dst_sel:DWORD dst_unused:UNUSED_PAD src0_sel:WORD_1
	v_cvt_f32_f16_e32 v6, v6
	global_store_dword v[12:13], v5, off
	v_mov_b32_e32 v12, v27
	v_pk_mul_f32 v[10:11], v[12:13], v[10:11] op_sel_hi:[0,1]
	s_mov_b32 s2, 0x70000
	v_pk_fma_f32 v[8:9], v[8:9], v[26:27], v[10:11] op_sel_hi:[1,0,1]
	v_add_co_u32_e32 v10, vcc, s2, v2
	s_waitcnt lgkmcnt(0)
	v_pk_mul_f32 v[6:7], v[28:29], v[6:7] op_sel:[1,0]
	v_addc_co_u32_e32 v11, vcc, 0, v3, vcc
	s_mov_b32 s2, 0x74000
	v_cvt_pk_f16_f32 v5, v8, v9
	v_pk_fma_f32 v[6:7], v[8:9], v[28:29], v[6:7] op_sel_hi:[1,0,1]
	s_waitcnt vmcnt(29)
	v_cvt_f32_f16_sdwa v9, v1 dst_sel:DWORD dst_unused:UNUSED_PAD src0_sel:WORD_1
	v_cvt_f32_f16_e32 v8, v1
	v_add_co_u32_e32 v12, vcc, s2, v2
	global_store_dword v[10:11], v5, off
	ds_read_b64 v[10:11], v97 offset:240
	v_cvt_pk_f16_f32 v5, v6, v7
	v_addc_co_u32_e32 v13, vcc, 0, v3, vcc
	global_store_dword v[12:13], v5, off
	s_waitcnt vmcnt(30)
	v_cvt_f32_f16_sdwa v5, v4 dst_sel:DWORD dst_unused:UNUSED_PAD src0_sel:WORD_1
	v_cvt_f32_f16_e32 v4, v4
	v_mov_b32_e32 v12, v31
	v_pk_mul_f32 v[8:9], v[12:13], v[8:9] op_sel_hi:[0,1]
	s_mov_b32 s2, 0x78000
	v_pk_fma_f32 v[6:7], v[6:7], v[30:31], v[8:9] op_sel_hi:[1,0,1]
	v_add_co_u32_e32 v8, vcc, s2, v2
	s_waitcnt lgkmcnt(0)
	v_pk_mul_f32 v[4:5], v[10:11], v[4:5] op_sel:[1,0]
	v_addc_co_u32_e32 v9, vcc, 0, v3, vcc
	s_cmp_eq_u32 s1, 0
	v_cvt_pk_f16_f32 v1, v6, v7
	v_pk_fma_f32 v[4:5], v[6:7], v[10:11], v[4:5] op_sel_hi:[1,0,1]
	v_add_co_u32_e32 v2, vcc, 0x7c000, v2
	s_cselect_b64 s[2:3], -1, 0
	global_store_dword v[8:9], v1, off
	v_cvt_pk_f16_f32 v1, v4, v5
	v_addc_co_u32_e32 v3, vcc, 0, v3, vcc
	s_and_b64 s[10:11], s[2:3], s[38:39]
	global_store_dword v[2:3], v1, off
	s_and_saveexec_b64 s[2:3], s[10:11]
	s_cbranch_execz .LBB0_755
; __device__ __forceinline__ void x2_item(int item, int b0, const h16* __restrict__ U, const float* __restrict__ un, const float* __restrict__ amax, const float* __restrict__ blast, ...
;     ...
;     if (sl == 0 && tid < 64) { float n = 0.f; ns[((size_t)gbh * 32) * 64 + tid] = 0.f;
;         float uv[31];
; #pragma unroll
;         for (int c = 0; c < 31; ++c) uv[c] = un[((size_t)gbh * 32 + c) * 64 + tid];
;         asm volatile("" ::: "memory");
; #pragma unroll
;         for (int c = 0; c < 31; ++c) { n = coef[2 * c] * n + coef[2 * c + 1] * uv[c]; ns[((size_t)gbh * 32 + c + 1) * 64 + tid] = n; } }
	s_waitcnt vmcnt(32)
	s_ashr_i32 s1, s0, 31
	s_lshl_b64 s[0:1], s[0:1], 13
	v_ashrrev_i32_e32 v1, 31, v0
	s_add_u32 s10, s92, s0
	s_addc_u32 s11, s93, s1
	v_lshlrev_b64 v[0:1], 2, v[0:1]
	v_lshl_add_u64 v[2:3], s[10:11], 0, v[0:1]
	v_readlane_b32 s10, v254, 30
	v_readlane_b32 s11, v254, 31
	s_or_b32 s64, s0, 0x1000
	s_mov_b32 s65, s1
	v_lshl_add_u64 v[4:5], s[10:11], 0, v[0:1]
	v_lshl_add_u64 v[6:7], v[4:5], 0, s[0:1]
	v_mov_b32_e32 v30, v200
	v_mov_b32_e32 v31, v201
	v_mov_b32_e32 v32, v202
	v_mov_b32_e32 v33, v203
	v_mov_b32_e32 v34, v204
	v_mov_b32_e32 v35, v205
	v_mov_b32_e32 v36, v206
	v_mov_b32_e32 v37, v207
	v_mov_b32_e32 v38, v208
	v_mov_b32_e32 v39, v209
	v_mov_b32_e32 v40, v210
	v_mov_b32_e32 v41, v211
	v_mov_b32_e32 v42, v212
	v_mov_b32_e32 v43, v213
	v_mov_b32_e32 v44, v214
	v_mov_b32_e32 v45, v215
	s_or_b32 s14, s0, 0x1700
	s_mov_b32 s15, s1
	v_lshl_add_u64 v[6:7], v[4:5], 0, s[64:65]
	s_or_b32 s62, s0, 0x1100
	s_mov_b32 s63, s1
	v_lshl_add_u64 v[8:9], v[4:5], 0, s[14:15]
	s_or_b32 s52, s0, 0x1800
	s_mov_b32 s53, s1
	v_mov_b32_e32 v46, v216
	v_mov_b32_e32 v13, v223
	v_lshl_add_u64 v[6:7], v[4:5], 0, s[62:63]
	s_or_b32 s60, s0, 0x1200
	s_mov_b32 s61, s1
	v_lshl_add_u64 v[8:9], v[4:5], 0, s[52:53]
	v_mov_b32_e32 v47, v217
	v_mov_b32_e32 v12, v224
	v_lshl_add_u64 v[6:7], v[4:5], 0, s[60:61]
	v_mov_b32_e32 v48, v218
	s_or_b32 s50, s0, 0x1900
	s_mov_b32 s51, s1
	s_or_b32 s58, s0, 0x1300
	s_mov_b32 s59, s1
	v_lshl_add_u64 v[8:9], v[4:5], 0, s[50:51]
	s_or_b32 s46, s0, 0x1a00
	s_mov_b32 s47, s1
	s_or_b32 s54, s0, 0x1400
	s_mov_b32 s55, s1
	v_mov_b32_e32 v11, v225
	v_lshl_add_u64 v[6:7], v[4:5], 0, s[58:59]
	v_lshl_add_u64 v[8:9], v[4:5], 0, s[46:47]
	s_or_b32 s42, s0, 0x1b00
	s_mov_b32 s43, s1
	v_mov_b32_e32 v49, v219
	v_mov_b32_e32 v10, v226
	v_lshl_add_u64 v[6:7], v[4:5], 0, s[54:55]
	s_or_b32 s56, s0, 0x1500
	s_mov_b32 s57, s1
	v_lshl_add_u64 v[8:9], v[4:5], 0, s[42:43]
	v_mov_b32_e32 v50, v220
	s_or_b32 s40, s0, 0x1c00
	v_mov_b32_e32 v9, v227
	v_lshl_add_u64 v[6:7], v[4:5], 0, s[56:57]
	v_mov_b32_e32 v51, v221
	s_mov_b32 s41, s1
	s_or_b32 s38, s0, 0x1600
	s_mov_b32 s39, s1
	v_lshl_add_u64 v[14:15], v[4:5], 0, s[40:41]
	v_mov_b32_e32 v8, v228
	v_lshl_add_u64 v[6:7], v[4:5], 0, s[38:39]
	v_mov_b32_e32 v7, v222
	s_or_b32 s44, s0, 0x100
	s_or_b32 s37, s0, 0x200
	s_or_b32 s36, s0, 0x300
	s_or_b32 s35, s0, 0x400
	s_or_b32 s34, s0, 0x500
	s_or_b32 s28, s0, 0x600
	s_or_b32 s19, s0, 0x700
	s_or_b32 s27, s0, 0x800
	s_or_b32 s26, s0, 0x900
	s_or_b32 s18, s0, 0xa00
	s_or_b32 s13, s0, 0xb00
	s_or_b32 s12, s0, 0xc00
	s_or_b32 s11, s0, 0xd00
	s_or_b32 s10, s0, 0xe00
	s_or_b32 s6, s0, 0xf00
	s_or_b32 s20, s0, 0x1d00
	s_mov_b32 s21, s1
	s_or_b32 s0, s0, 0x1e00
	v_lshl_add_u64 v[14:15], v[4:5], 0, s[20:21]
	v_lshl_add_u64 v[4:5], v[4:5], 0, s[0:1]
	v_mov_b32_e32 v4, v230
	s_add_u32 s44, s92, s44
	v_mov_b32_e32 v6, v229
	s_addc_u32 s45, s93, s1
	global_store_dword v[2:3], v97, off
	ds_read_b128 v[14:17], v97
	ds_read_b128 v[18:21], v97 offset:16
	ds_read_b128 v[22:25], v97 offset:32
	ds_read_b128 v[26:29], v97 offset:48
	s_waitcnt vmcnt(31) lgkmcnt(3)
	v_mul_f32_e32 v5, v30, v15
	v_fmac_f32_e32 v5, 0, v14
	global_store_dword v[2:3], v5, off offset:256
	v_lshl_add_u64 v[2:3], s[44:45], 0, v[0:1]
	s_add_u32 s44, s92, s37
	s_waitcnt vmcnt(31)
	v_mul_f32_e32 v14, v31, v17
	s_addc_u32 s45, s93, s1
	v_fmac_f32_e32 v14, v5, v16
	s_waitcnt vmcnt(30) lgkmcnt(2)
	v_mul_f32_e32 v5, v32, v19
	s_add_u32 s36, s92, s36
	global_store_dword v[2:3], v14, off offset:256
	v_fmac_f32_e32 v5, v14, v18
	v_lshl_add_u64 v[2:3], s[44:45], 0, v[0:1]
	s_addc_u32 s37, s93, s1
	global_store_dword v[2:3], v5, off offset:256
	v_lshl_add_u64 v[2:3], s[36:37], 0, v[0:1]
	s_add_u32 s36, s92, s35
	s_waitcnt vmcnt(31)
	v_mul_f32_e32 v14, v33, v21
	s_addc_u32 s37, s93, s1
	v_fmac_f32_e32 v14, v5, v20
	s_waitcnt vmcnt(30) lgkmcnt(1)
	v_mul_f32_e32 v5, v34, v23
	s_add_u32 s34, s92, s34
	global_store_dword v[2:3], v14, off offset:256
	v_fmac_f32_e32 v5, v14, v22
	v_lshl_add_u64 v[2:3], s[36:37], 0, v[0:1]
	s_waitcnt vmcnt(30)
	v_mul_f32_e32 v14, v35, v25
	s_addc_u32 s35, s93, s1
	global_store_dword v[2:3], v5, off offset:256
	v_fmac_f32_e32 v14, v5, v24
	v_lshl_add_u64 v[2:3], s[34:35], 0, v[0:1]
	s_waitcnt vmcnt(30) lgkmcnt(0)
	v_mul_f32_e32 v5, v36, v27
	global_store_dword v[2:3], v14, off offset:256
	v_fmac_f32_e32 v5, v14, v26
	ds_read_b128 v[14:17], v97 offset:64
	s_add_u32 s34, s92, s28
	s_addc_u32 s35, s93, s1
	v_lshl_add_u64 v[2:3], s[34:35], 0, v[0:1]
	s_add_u32 s34, s92, s19
	s_waitcnt vmcnt(30)
	v_mul_f32_e32 v18, v37, v29
	s_addc_u32 s35, s93, s1
	global_store_dword v[2:3], v5, off offset:256
	v_fmac_f32_e32 v18, v5, v28
	v_lshl_add_u64 v[2:3], s[34:35], 0, v[0:1]
	s_waitcnt vmcnt(30) lgkmcnt(0)
	v_mul_f32_e32 v5, v38, v15
	global_store_dword v[2:3], v18, off offset:256
	v_fmac_f32_e32 v5, v18, v14
	s_add_u32 s34, s92, s27
	s_waitcnt vmcnt(30)
	v_mul_f32_e32 v18, v39, v17
	s_addc_u32 s35, s93, s1
	v_fmac_f32_e32 v18, v5, v16
	ds_read_b128 v[14:17], v97 offset:80
	s_add_u32 s26, s92, s26
	s_addc_u32 s27, s93, s1
	v_lshl_add_u64 v[2:3], s[34:35], 0, v[0:1]
	s_add_u32 s18, s92, s18
	global_store_dword v[2:3], v5, off offset:256
	v_lshl_add_u64 v[2:3], s[26:27], 0, v[0:1]
	s_addc_u32 s19, s93, s1
	global_store_dword v[2:3], v18, off offset:256
	s_waitcnt vmcnt(31) lgkmcnt(0)
; __device__ __forceinline__ void x2_item(int item, int b0, const h16* __restrict__ U, const float* __restrict__ un, const float* __restrict__ amax, const float* __restrict__ blast, ...
;     ...
;     if (sl == 0 && tid < 64) { float n = 0.f; ns[((size_t)gbh * 32) * 64 + tid] = 0.f;
;         float uv[31];
; #pragma unroll
;         for (int c = 0; c < 31; ++c) uv[c] = un[((size_t)gbh * 32 + c) * 64 + tid];
;         asm volatile("" ::: "memory");
; #pragma unroll
;         for (int c = 0; c < 31; ++c) { n = coef[2 * c] * n + coef[2 * c + 1] * uv[c]; ns[((size_t)gbh * 32 + c + 1) * 64 + tid] = n; } }
;     __syncthreads();
	v_mul_f32_e32 v5, v40, v15
	v_lshl_add_u64 v[2:3], s[18:19], 0, v[0:1]
	s_add_u32 s18, s92, s13
	v_fmac_f32_e32 v5, v18, v14
	s_waitcnt vmcnt(30)
	v_mul_f32_e32 v30, v41, v17
	s_addc_u32 s19, s93, s1
	global_store_dword v[2:3], v5, off offset:256
	v_fmac_f32_e32 v30, v5, v16
	v_lshl_add_u64 v[2:3], s[18:19], 0, v[0:1]
	global_store_dword v[2:3], v30, off offset:256
	s_add_u32 s12, s92, s12
	ds_read_b128 v[14:17], v97 offset:96
	ds_read_b128 v[18:21], v97 offset:112
	ds_read_b128 v[22:25], v97 offset:128
	ds_read_b128 v[26:29], v97 offset:144
	s_addc_u32 s13, s93, s1
	v_lshl_add_u64 v[2:3], s[12:13], 0, v[0:1]
	s_add_u32 s12, s92, s11
	s_waitcnt vmcnt(31) lgkmcnt(3)
	v_mul_f32_e32 v5, v42, v15
	s_addc_u32 s13, s93, s1
	v_fmac_f32_e32 v5, v30, v14
	s_waitcnt vmcnt(30)
	v_mul_f32_e32 v14, v43, v17
	s_add_u32 s10, s92, s10
	global_store_dword v[2:3], v5, off offset:256
	v_fmac_f32_e32 v14, v5, v16
	v_lshl_add_u64 v[2:3], s[12:13], 0, v[0:1]
	s_addc_u32 s11, s93, s1
	global_store_dword v[2:3], v14, off offset:256
	s_waitcnt vmcnt(31) lgkmcnt(2)
	v_mul_f32_e32 v5, v44, v19
	v_lshl_add_u64 v[2:3], s[10:11], 0, v[0:1]
	s_add_u32 s10, s92, s6
	v_fmac_f32_e32 v5, v14, v18
	s_addc_u32 s11, s93, s1
	global_store_dword v[2:3], v5, off offset:256
	s_waitcnt vmcnt(31)
	v_mul_f32_e32 v14, v45, v21
	v_lshl_add_u64 v[2:3], s[10:11], 0, v[0:1]
	s_add_u32 s10, s92, s64
	v_fmac_f32_e32 v14, v5, v20
	s_addc_u32 s11, s93, s1
	global_store_dword v[2:3], v14, off offset:256
	s_waitcnt vmcnt(31) lgkmcnt(1)
	v_mul_f32_e32 v5, v46, v23
	v_lshl_add_u64 v[2:3], s[10:11], 0, v[0:1]
	s_add_u32 s10, s92, s62
	v_fmac_f32_e32 v5, v14, v22
	s_waitcnt vmcnt(29)
	v_mul_f32_e32 v14, v47, v25
	s_addc_u32 s11, s93, s1
	global_store_dword v[2:3], v5, off offset:256
	v_fmac_f32_e32 v14, v5, v24
	v_lshl_add_u64 v[2:3], s[10:11], 0, v[0:1]
	s_waitcnt vmcnt(28) lgkmcnt(0)
	v_mul_f32_e32 v5, v48, v27
	global_store_dword v[2:3], v14, off offset:256
	v_fmac_f32_e32 v5, v14, v26
	ds_read_b128 v[14:17], v97 offset:160
	s_add_u32 s10, s92, s60
	s_addc_u32 s11, s93, s1
	v_lshl_add_u64 v[2:3], s[10:11], 0, v[0:1]
	s_add_u32 s10, s92, s58
	s_waitcnt vmcnt(27)
	v_mul_f32_e32 v18, v49, v29
	s_addc_u32 s11, s93, s1
	global_store_dword v[2:3], v5, off offset:256
	v_fmac_f32_e32 v18, v5, v28
	v_lshl_add_u64 v[2:3], s[10:11], 0, v[0:1]
	s_waitcnt vmcnt(26) lgkmcnt(0)
	v_mul_f32_e32 v5, v50, v15
	global_store_dword v[2:3], v18, off offset:256
	v_fmac_f32_e32 v5, v18, v14
	s_add_u32 s10, s92, s54
	s_waitcnt vmcnt(25)
	v_mul_f32_e32 v18, v51, v17
	s_addc_u32 s11, s93, s1
	v_fmac_f32_e32 v18, v5, v16
	ds_read_b128 v[14:17], v97 offset:176
	v_lshl_add_u64 v[2:3], s[10:11], 0, v[0:1]
	s_add_u32 s10, s92, s56
	s_addc_u32 s11, s93, s1
	global_store_dword v[2:3], v5, off offset:256
	v_lshl_add_u64 v[2:3], s[10:11], 0, v[0:1]
	s_add_u32 s10, s92, s38
	s_addc_u32 s11, s93, s1
	global_store_dword v[2:3], v18, off offset:256
	s_waitcnt vmcnt(25) lgkmcnt(0)
	v_mul_f32_e32 v5, v7, v15
	v_lshl_add_u64 v[2:3], s[10:11], 0, v[0:1]
	s_add_u32 s10, s92, s14
	v_fmac_f32_e32 v5, v18, v14
	v_mul_f32_e32 v7, v13, v17
	s_addc_u32 s11, s93, s1
	global_store_dword v[2:3], v5, off offset:256
	v_fmac_f32_e32 v7, v5, v16
	v_lshl_add_u64 v[2:3], s[10:11], 0, v[0:1]
	global_store_dword v[2:3], v7, off offset:256
	ds_read_b128 v[14:17], v97 offset:192
	ds_read_b128 v[18:21], v97 offset:208
	ds_read_b128 v[22:25], v97 offset:224
	ds_read_b64 v[2:3], v97 offset:240
	s_add_u32 s10, s92, s52
	s_addc_u32 s11, s93, s1
	s_waitcnt lgkmcnt(3)
	v_mul_f32_e32 v5, v12, v15
	v_lshl_add_u64 v[12:13], s[10:11], 0, v[0:1]
	s_add_u32 s10, s92, s50
	v_fmac_f32_e32 v5, v7, v14
	s_addc_u32 s11, s93, s1
	global_store_dword v[12:13], v5, off offset:256
	v_lshl_add_u64 v[12:13], s[10:11], 0, v[0:1]
	s_add_u32 s10, s92, s46
	v_mul_f32_e32 v7, v11, v17
	s_addc_u32 s11, s93, s1
	v_fmac_f32_e32 v7, v5, v16
	s_waitcnt lgkmcnt(2)
	v_mul_f32_e32 v5, v10, v19
	v_lshl_add_u64 v[10:11], s[10:11], 0, v[0:1]
	s_add_u32 s10, s92, s42
	v_fmac_f32_e32 v5, v7, v18
	s_addc_u32 s11, s93, s1
	global_store_dword v[10:11], v5, off offset:256
	v_lshl_add_u64 v[10:11], s[10:11], 0, v[0:1]
	s_add_u32 s10, s92, s40
	global_store_dword v[12:13], v7, off offset:256
	v_mul_f32_e32 v7, v9, v21
	s_addc_u32 s11, s93, s1
	v_fmac_f32_e32 v7, v5, v20
	s_waitcnt lgkmcnt(1)
	v_mul_f32_e32 v5, v8, v23
	v_lshl_add_u64 v[8:9], s[10:11], 0, v[0:1]
	s_add_u32 s10, s92, s20
	v_fmac_f32_e32 v5, v7, v22
	s_addc_u32 s11, s93, s1
	global_store_dword v[8:9], v5, off offset:256
	s_waitcnt vmcnt(29)
	v_mul_f32_e32 v8, v6, v25
	s_add_u32 s0, s92, s0
	v_fmac_f32_e32 v8, v5, v24
	s_waitcnt lgkmcnt(0)
	v_mul_f32_e32 v3, v4, v3
	s_addc_u32 s1, s93, s1
	s_mov_b32 s44, 0x800000
	s_movk_i32 s27, 0x2000
	s_mov_b64 s[62:63], 0x80
	v_readlane_b32 s45, v255, 35
	global_store_dword v[10:11], v7, off offset:256
	v_lshl_add_u64 v[6:7], s[10:11], 0, v[0:1]
	v_fmac_f32_e32 v3, v8, v2
	v_lshl_add_u64 v[0:1], s[0:1], 0, v[0:1]
	global_store_dword v[6:7], v8, off offset:256
	global_store_dword v[0:1], v3, off offset:256
	s_branch .LBB0_755
